# v037 + P13 tile DMA issue moved from behind the barrier into the QK MFMA result wait
# baseline (speedup 1.0000x reference)
.LBB0_2751:
	ds_read_b64 v[226:227], v146
	v_add_u32_e32 v179, s39, v151
	v_add_u32_e32 v225, v179, v155
	v_add_u32_e32 v224, v179, v181
	v_add_u32_e32 v223, v179, v219
	s_waitcnt lgkmcnt(0)
	v_lshrrev_b32_e32 v82, v163, v226
	v_bfe_i32 v83, v82, 26, 1
	v_bitop3_b32 v96, v16, s28, v83 bitop3:0xe4
	v_bfe_i32 v83, v82, 25, 1
	v_bitop3_b32 v95, v13, s28, v83 bitop3:0xe4
	v_bfe_i32 v83, v82, 24, 1
	v_bitop3_b32 v94, v14, s28, v83 bitop3:0xe4
	v_bfe_i32 v83, v82, 19, 1
	v_bitop3_b32 v93, v11, s28, v83 bitop3:0xe4
	v_bfe_i32 v83, v82, 18, 1
	v_bitop3_b32 v92, v12, s28, v83 bitop3:0xe4
	v_bfe_i32 v83, v82, 17, 1
	v_add_u32_e32 v226, v179, v153
	v_bitop3_b32 v91, v9, s28, v83 bitop3:0xe4
	v_bfe_i32 v83, v82, 16, 1
	ds_read_b128 v[186:189], v226
	v_bitop3_b32 v90, v10, s28, v83 bitop3:0xe4
	v_bfe_i32 v83, v82, 11, 1
	v_bitop3_b32 v89, v7, s28, v83 bitop3:0xe4
	v_bfe_i32 v83, v82, 10, 1
	v_bitop3_b32 v88, v8, s28, v83 bitop3:0xe4
	v_bfe_i32 v83, v82, 9, 1
	v_bitop3_b32 v87, v5, s28, v83 bitop3:0xe4
	v_bfe_i32 v83, v82, 8, 1
	v_bitop3_b32 v86, v6, s28, v83 bitop3:0xe4
	v_bfe_i32 v83, v82, 3, 1
	v_bfe_i32 v84, v82, 27, 1
	v_bitop3_b32 v85, v3, s28, v83 bitop3:0xe4
	v_bfe_i32 v83, v82, 2, 1
	v_bitop3_b32 v97, v15, s28, v84 bitop3:0xe4
	v_bitop3_b32 v84, v4, s28, v83 bitop3:0xe4
	v_bfe_i32 v83, v82, 1, 1
	v_bfe_i32 v82, v82, 0, 1
	v_bitop3_b32 v83, v1, s28, v83 bitop3:0xe4
	v_bitop3_b32 v82, v2, s28, v82 bitop3:0xe4
	v_add_u32_e32 v179, s39, v17
	s_waitcnt lgkmcnt(0)
	v_mfma_f32_32x32x16_bf16 v[98:113], v[186:189], v[114:117], v[82:97]
	v_add_u32_e32 v146, 8, v146
	v_mfma_f32_32x32x16_bf16 v[82:97], v[186:189], v[130:133], v[82:97]
	ds_read_b128 v[186:189], v225
	s_waitcnt lgkmcnt(0)
	v_mfma_f32_32x32x16_bf16 v[98:113], v[186:189], v[118:121], v[98:113]
	v_mfma_f32_32x32x16_bf16 v[82:97], v[186:189], v[134:137], v[82:97]
	ds_read_b128 v[186:189], v224
	s_waitcnt lgkmcnt(0)
	v_mfma_f32_32x32x16_bf16 v[98:113], v[186:189], v[122:125], v[98:113]
	v_mfma_f32_32x32x16_bf16 v[82:97], v[186:189], v[138:141], v[82:97]
	ds_read_b128 v[186:189], v223
	s_waitcnt lgkmcnt(0)
	v_mfma_f32_32x32x16_bf16 v[98:113], v[186:189], v[126:129], v[98:113]
	v_mfma_f32_32x32x16_bf16 v[82:97], v[186:189], v[142:145], v[82:97]
	s_cmp_le_u32 s38, s34
	s_cbranch_scc0 .Lp13_nodma
	s_add_i32 s14, s39, 0xffffc000
	s_cmp_lg_u32 s37, 0
	s_cselect_b32 s40, s14, 0x8000
	v_lshl_add_u64 v[240:241], v[182:183], 0, s[0:1]
	s_mov_b64 s[14:15], 0x39208000
	s_add_i32 s40, s22, s40
	v_lshl_add_u64 v[242:243], v[240:241], 0, s[14:15]
	s_mov_b32 m0, s40
	s_mov_b64 s[14:15], 0x39208080
	global_load_lds_dwordx4 v[242:243], off
	v_lshl_add_u64 v[240:241], v[240:241], 0, s[14:15]
	s_add_i32 m0, s40, 0x2000
	s_mov_b64 s[14:15], 0x3a208000
	global_load_lds_dwordx4 v[240:241], off
	v_lshl_add_u64 v[240:241], v[172:173], 0, s[0:1]
	v_lshl_add_u64 v[242:243], v[240:241], 0, s[14:15]
	s_add_i32 m0, s40, 0xc000
	v_lshl_add_u64 v[240:241], v[240:241], 0, s[12:13]
	global_load_lds_dwordx4 v[242:243], off
	s_add_i32 m0, s40, 0xe000
	s_nop 0
	global_load_lds_dwordx4 v[240:241], off
	s_branch .Lp13_dmadone
.Lp13_nodma:
	s_nop 10
.Lp13_dmadone:
	s_add_i32 s14, s37, 1
	s_cmp_lg_u32 s37, 2
	s_cselect_b32 s37, s14, 0
	s_add_u32 s0, s0, 0x4000
	s_addc_u32 s1, s1, 0
	s_add_i32 s38, s38, 1
	s_cmp_eq_u32 s36, s0
	v_exp_f32_e32 v190, v98
	v_exp_f32_e32 v191, v99
	v_exp_f32_e32 v192, v100
	v_exp_f32_e32 v193, v101
	s_nop 0
	ds_read_b64_tr_b16 v[98:99], v179 offset:49152
	ds_read_b64_tr_b16 v[100:101], v179 offset:50176
	v_exp_f32_e32 v188, v102
	v_exp_f32_e32 v189, v103
	v_exp_f32_e32 v186, v104
	v_exp_f32_e32 v187, v105
	ds_read_b64_tr_b16 v[212:213], v179 offset:50688
	ds_read_b64_tr_b16 v[210:211], v179 offset:49664
	v_exp_f32_e32 v204, v82
	v_exp_f32_e32 v205, v83
	v_exp_f32_e32 v208, v84
	v_exp_f32_e32 v209, v85
	v_exp_f32_e32 v200, v86
	v_exp_f32_e32 v201, v87
	v_exp_f32_e32 v196, v88
	v_exp_f32_e32 v197, v89
	v_cvt_pk_bf16_f32 v102, v190, v191
	v_cvt_pk_bf16_f32 v103, v192, v193
	v_cvt_pk_bf16_f32 v104, v188, v189
	v_cvt_pk_bf16_f32 v105, v186, v187
	v_cvt_pk_bf16_f32 v82, v204, v205
	v_cvt_pk_bf16_f32 v83, v208, v209
	s_waitcnt lgkmcnt(2)
	v_mfma_f32_32x32x16_bf16 v[66:81], v[98:101], v[102:105], v[66:81]
	v_cvt_pk_bf16_f32 v84, v200, v201
	v_cvt_pk_bf16_f32 v85, v196, v197
	v_exp_f32_e32 v206, v106
	v_exp_f32_e32 v207, v107
	v_exp_f32_e32 v202, v108
	v_exp_f32_e32 v203, v109
	v_exp_f32_e32 v198, v110
	s_waitcnt lgkmcnt(0)
	v_mfma_f32_32x32x16_bf16 v[50:65], v[210:213], v[102:105], v[50:65]
	v_exp_f32_e32 v199, v111
	v_exp_f32_e32 v194, v112
	v_exp_f32_e32 v195, v113
	v_exp_f32_e32 v216, v90
	v_exp_f32_e32 v217, v91
	v_exp_f32_e32 v214, v92
	v_exp_f32_e32 v215, v93
	v_mfma_f32_32x32x16_bf16 v[34:49], v[98:101], v[82:85], v[34:49]
	v_cvt_pk_bf16_f32 v86, v206, v207
	v_cvt_pk_bf16_f32 v87, v202, v203
	v_cvt_pk_bf16_f32 v88, v198, v199
	v_cvt_pk_bf16_f32 v89, v194, v195
	v_mfma_f32_32x32x16_bf16 v[18:33], v[210:213], v[82:85], v[18:33]
	ds_read_b64_tr_b16 v[82:83], v179 offset:51200
	ds_read_b64_tr_b16 v[84:85], v179 offset:52224
	ds_read_b64_tr_b16 v[100:101], v179 offset:52736
	ds_read_b64_tr_b16 v[98:99], v179 offset:51712
	v_exp_f32_e32 v212, v94
	v_exp_f32_e32 v213, v95
	v_exp_f32_e32 v210, v96
	v_exp_f32_e32 v211, v97
	s_waitcnt lgkmcnt(2)
	v_mfma_f32_32x32x16_bf16 v[66:81], v[82:85], v[86:89], v[66:81]
	s_waitcnt lgkmcnt(0)
	v_mfma_f32_32x32x16_bf16 v[50:65], v[98:101], v[86:89], v[50:65]
	v_cvt_pk_bf16_f32 v86, v216, v217
	v_cvt_pk_bf16_f32 v87, v214, v215
	v_cvt_pk_bf16_f32 v88, v212, v213
	v_cvt_pk_bf16_f32 v89, v210, v211
	s_nop 1
	v_mfma_f32_32x32x16_bf16 v[34:49], v[82:85], v[86:89], v[34:49]
	v_lshrrev_b32_e32 v82, v163, v227
	v_bfe_i32 v83, v82, 26, 1
	v_bitop3_b32 v96, v16, s28, v83 bitop3:0xe4
	v_bfe_i32 v83, v82, 25, 1
	v_bitop3_b32 v95, v13, s28, v83 bitop3:0xe4
	v_bfe_i32 v83, v82, 24, 1
	v_bitop3_b32 v94, v14, s28, v83 bitop3:0xe4
	v_bfe_i32 v83, v82, 19, 1
	v_bitop3_b32 v93, v11, s28, v83 bitop3:0xe4
	v_bfe_i32 v83, v82, 18, 1
	v_bitop3_b32 v92, v12, s28, v83 bitop3:0xe4
	v_bfe_i32 v83, v82, 17, 1
	v_bitop3_b32 v91, v9, s28, v83 bitop3:0xe4
	v_bfe_i32 v83, v82, 16, 1
	ds_read_b128 v[226:229], v226 offset:4096
	v_bitop3_b32 v90, v10, s28, v83 bitop3:0xe4
	v_bfe_i32 v83, v82, 11, 1
	v_mfma_f32_32x32x16_bf16 v[18:33], v[98:101], v[86:89], v[18:33]
	v_bitop3_b32 v89, v7, s28, v83 bitop3:0xe4
	v_bfe_i32 v83, v82, 10, 1
	v_bitop3_b32 v88, v8, s28, v83 bitop3:0xe4
	v_bfe_i32 v83, v82, 9, 1
	v_bitop3_b32 v87, v5, s28, v83 bitop3:0xe4
	v_bfe_i32 v83, v82, 8, 1
	v_bitop3_b32 v86, v6, s28, v83 bitop3:0xe4
	v_bfe_i32 v83, v82, 3, 1
	v_bfe_i32 v84, v82, 27, 1
	v_bitop3_b32 v85, v3, s28, v83 bitop3:0xe4
	v_bfe_i32 v83, v82, 2, 1
	v_bitop3_b32 v97, v15, s28, v84 bitop3:0xe4
	v_bitop3_b32 v84, v4, s28, v83 bitop3:0xe4
	v_bfe_i32 v83, v82, 1, 1
	v_bfe_i32 v82, v82, 0, 1
	v_bitop3_b32 v83, v1, s28, v83 bitop3:0xe4
	v_bitop3_b32 v82, v2, s28, v82 bitop3:0xe4
	s_waitcnt lgkmcnt(0)
	s_nop 0
	v_mfma_f32_32x32x16_bf16 v[98:113], v[226:229], v[114:117], v[82:97]
	v_mfma_f32_32x32x16_bf16 v[82:97], v[226:229], v[130:133], v[82:97]
	ds_read_b128 v[226:229], v225 offset:4096
	s_waitcnt lgkmcnt(0)
	v_mfma_f32_32x32x16_bf16 v[98:113], v[226:229], v[118:121], v[98:113]
	v_mfma_f32_32x32x16_bf16 v[82:97], v[226:229], v[134:137], v[82:97]
	ds_read_b128 v[224:227], v224 offset:4096
	s_waitcnt lgkmcnt(0)
	v_mfma_f32_32x32x16_bf16 v[98:113], v[224:227], v[122:125], v[98:113]
	v_mfma_f32_32x32x16_bf16 v[82:97], v[224:227], v[138:141], v[82:97]
	ds_read_b128 v[224:227], v223 offset:4096
	s_waitcnt lgkmcnt(0)
	v_mfma_f32_32x32x16_bf16 v[98:113], v[224:227], v[126:129], v[98:113]
	v_mfma_f32_32x32x16_bf16 v[82:97], v[224:227], v[142:145], v[82:97]
	s_nop 10
	v_exp_f32_e32 v228, v98
	v_exp_f32_e32 v229, v99
	v_exp_f32_e32 v230, v100
	v_exp_f32_e32 v231, v101
	ds_read_b64_tr_b16 v[98:99], v179 offset:53248
	ds_read_b64_tr_b16 v[100:101], v179 offset:54272
	v_exp_f32_e32 v232, v102
	v_exp_f32_e32 v233, v103
	v_exp_f32_e32 v234, v104
	v_exp_f32_e32 v235, v105
	ds_read_b64_tr_b16 v[226:227], v179 offset:54784
	ds_read_b64_tr_b16 v[224:225], v179 offset:53760
	v_cvt_pk_bf16_f32 v102, v228, v229
	v_cvt_pk_bf16_f32 v103, v230, v231
	v_cvt_pk_bf16_f32 v104, v232, v233
	v_cvt_pk_bf16_f32 v105, v234, v235
	v_exp_f32_e32 v236, v86
	v_exp_f32_e32 v237, v87
	s_waitcnt lgkmcnt(2)
	v_mfma_f32_32x32x16_bf16 v[66:81], v[98:101], v[102:105], v[66:81]
	v_exp_f32_e32 v238, v88
	v_exp_f32_e32 v239, v89
	v_exp_f32_e32 v106, v106
	v_exp_f32_e32 v107, v107
	v_exp_f32_e32 v108, v108
	v_exp_f32_e32 v109, v109
	v_exp_f32_e32 v110, v110
	s_waitcnt lgkmcnt(0)
	v_mfma_f32_32x32x16_bf16 v[50:65], v[224:227], v[102:105], v[50:65]
	v_exp_f32_e32 v102, v82
	v_exp_f32_e32 v103, v83
	v_exp_f32_e32 v104, v84
	v_exp_f32_e32 v105, v85
	v_cvt_pk_bf16_f32 v84, v236, v237
	v_cvt_pk_bf16_f32 v82, v102, v103
	v_cvt_pk_bf16_f32 v85, v238, v239
	v_cvt_pk_bf16_f32 v83, v104, v105
	v_exp_f32_e32 v111, v111
	v_exp_f32_e32 v112, v112
	v_mfma_f32_32x32x16_bf16 v[34:49], v[98:101], v[82:85], v[34:49]
	v_exp_f32_e32 v113, v113
	v_exp_f32_e32 v90, v90
	v_exp_f32_e32 v91, v91
	v_exp_f32_e32 v92, v92
	v_exp_f32_e32 v93, v93
	v_exp_f32_e32 v94, v94
	v_exp_f32_e32 v95, v95
	v_mfma_f32_32x32x16_bf16 v[18:33], v[224:227], v[82:85], v[18:33]
	ds_read_b64_tr_b16 v[82:83], v179 offset:55296
	ds_read_b64_tr_b16 v[84:85], v179 offset:56320
	ds_read_b64_tr_b16 v[100:101], v179 offset:56832
	ds_read_b64_tr_b16 v[98:99], v179 offset:55808
	v_exp_f32_e32 v96, v96
	v_exp_f32_e32 v97, v97
	v_cvt_pk_bf16_f32 v86, v106, v107
	v_cvt_pk_bf16_f32 v87, v108, v109
	v_cvt_pk_bf16_f32 v88, v110, v111
	v_cvt_pk_bf16_f32 v89, v112, v113
	s_waitcnt lgkmcnt(2)
	s_nop 0
	v_mfma_f32_32x32x16_bf16 v[66:81], v[82:85], v[86:89], v[66:81]
	s_waitcnt lgkmcnt(0)
	v_mfma_f32_32x32x16_bf16 v[50:65], v[98:101], v[86:89], v[50:65]
	v_cvt_pk_bf16_f32 v86, v90, v91
	v_cvt_pk_bf16_f32 v87, v92, v93
	v_cvt_pk_bf16_f32 v88, v94, v95
	v_cvt_pk_bf16_f32 v89, v96, v97
	s_nop 1
	v_mfma_f32_32x32x16_bf16 v[34:49], v[82:85], v[86:89], v[34:49]
	v_add_f32_e64 v82, v190, 0
	v_add_f32_e64 v83, v191, 0
	v_add_f32_e64 v84, v228, 0
	v_add_f32_e64 v85, v229, 0
	v_add_f32_e64 v82, v192, v82
	v_add_f32_e64 v83, v193, v83
	v_pk_add_f32 v[84:85], v[230:231], v[84:85]
	v_pk_add_f32 v[82:83], v[188:189], v[82:83]
	v_pk_add_f32 v[84:85], v[232:233], v[84:85]
	v_pk_add_f32 v[82:83], v[186:187], v[82:83]
	v_mfma_f32_32x32x16_bf16 v[18:33], v[98:101], v[86:89], v[18:33]
	v_add_f32_e64 v86, v204, 0
	v_add_f32_e64 v87, v205, 0
	v_add_f32_e64 v88, v102, 0
	v_add_f32_e64 v89, v103, 0
	v_add_f32_e64 v86, v208, v86
	v_add_f32_e64 v87, v209, v87
	v_pk_add_f32 v[88:89], v[104:105], v[88:89]
	v_pk_add_f32 v[86:87], v[200:201], v[86:87]
	v_pk_add_f32 v[88:89], v[236:237], v[88:89]
	v_pk_add_f32 v[84:85], v[234:235], v[84:85]
	v_pk_add_f32 v[86:87], v[196:197], v[86:87]
	v_pk_add_f32 v[88:89], v[238:239], v[88:89]
	v_pk_add_f32 v[82:83], v[206:207], v[82:83]
	v_pk_add_f32 v[84:85], v[106:107], v[84:85]
	v_pk_add_f32 v[86:87], v[216:217], v[86:87]
	v_pk_add_f32 v[88:89], v[90:91], v[88:89]
	v_pk_add_f32 v[82:83], v[202:203], v[82:83]
	v_pk_add_f32 v[84:85], v[108:109], v[84:85]
	v_pk_add_f32 v[86:87], v[214:215], v[86:87]
	v_pk_add_f32 v[88:89], v[92:93], v[88:89]
	v_pk_add_f32 v[82:83], v[198:199], v[82:83]
	v_pk_add_f32 v[84:85], v[110:111], v[84:85]
	v_pk_add_f32 v[86:87], v[212:213], v[86:87]
	v_pk_add_f32 v[88:89], v[94:95], v[88:89]
	v_pk_add_f32 v[82:83], v[194:195], v[82:83]
	v_pk_add_f32 v[84:85], v[112:113], v[84:85]
	v_pk_add_f32 v[86:87], v[210:211], v[86:87]
	v_pk_add_f32 v[88:89], v[96:97], v[88:89]
	v_pk_add_f32 v[82:83], v[82:83], v[84:85]
	v_pk_add_f32 v[84:85], v[86:87], v[88:89]
	v_mov_b32_e32 v86, v82
	v_mov_b32_e32 v87, v84
	v_mov_b32_e32 v84, v83
	v_pk_add_f32 v[82:83], v[86:87], v[84:85]
	s_nop 0
	v_pk_add_f32 v[184:185], v[184:185], v[82:83]
	s_cbranch_scc1 .LBB0_2745

.LBB0_2756:
	s_barrier
	s_lshl_b32 s39, s37, 14
	s_branch .LBB0_2751
